# MoBA: wave 0 issues 8 one-dword loads on the next unit Q rows and first two K/V tiles (L2 prefetch into a dead VGPR) after the tile loop, hiding part of the next unit prologue vmcnt(0) stall
# speedup vs baseline: 1.0123x; 1.0013x over previous
.LBB0_501:
	s_lshr_b32 s50, s49, 2
	s_waitcnt vmcnt(0) lgkmcnt(0)
	s_barrier
	v_readlane_b32 s92, v254, 41
	s_nop 3
	s_cmp_lg_u32 s92, 0
	s_cbranch_scc1 .Lpf0_done
	v_readlane_b32 s92, v194, 0
	v_readlane_b32 s64, v254, 46
	v_readlane_b32 s65, v254, 47
	s_nop 3
	s_cmp_ge_u32 s92, 0x800
	s_cbranch_scc1 .Lpf0_done
	s_and_b32 s93, s92, 15
	s_lshl_b32 s93, s93, 7
	s_bfe_u32 s94, s92, 0x40004
	s_mul_i32 s94, s94, 0xc00000
	s_add_u32 s93, s94, s93
	s_add_u32 s64, s64, s93
	s_addc_u32 s65, s65, 0
	s_lshr_b32 s93, s92, 8
	s_sub_i32 s93, 7, s93
	s_mul_i32 s93, s93, 0x180000
	v_mbcnt_lo_u32_b32 v250, -1, 0
	v_mbcnt_hi_u32_b32 v250, -1, v250
	v_mul_u32_u24_e32 v251, 0x1800, v250
	v_add_u32_e32 v252, 0x60000, v251
	s_nop 1
	global_load_dword v253, v251, s[64:65] offset:2048
	global_load_dword v253, v252, s[64:65] offset:2048
	v_add_u32_e32 v250, 0x1000, v251
	v_add_u32_e32 v252, 0x1000, v252
	global_load_dword v253, v250, s[64:65]
	global_load_dword v253, v252, s[64:65]
	v_add_u32_e32 v251, s93, v251
	v_add_u32_e32 v252, 0x60000, v251
	global_load_dword v253, v251, s[64:65]
	global_load_dword v253, v252, s[64:65]
	v_add_u32_e32 v251, 0xc0000, v251
	v_add_u32_e32 v252, 0xc0000, v252
	global_load_dword v253, v251, s[64:65]
	global_load_dword v253, v252, s[64:65]
.Lpf0_done:
	s_cmp_eq_u32 s50, s30
	s_cselect_b64 s[0:1], -1, 0
	s_mov_b64 s[46:47], -1
	s_and_b64 vcc, exec, s[0:1]
	s_cbranch_vccnz .LBB0_504
	v_bfe_u32 v32, v198, s50, 1
	v_cmp_ne_u32_e32 vcc, 0, v32
	s_cmp_lg_u64 vcc, 0
	s_cselect_b64 s[6:7], -1, 0
	s_lshl_b32 s30, s49, 6
	s_cbranch_execz .LBB0_505

.LBB0_3040:
	s_lshr_b32 s39, s38, 2
	s_waitcnt vmcnt(0) lgkmcnt(0)
	s_barrier
	v_readlane_b32 s92, v254, 41
	s_nop 3
	s_cmp_lg_u32 s92, 0
	s_cbranch_scc1 .Lpf1_done
	v_readlane_b32 s92, v194, 0
	v_readlane_b32 s64, v254, 46
	v_readlane_b32 s65, v254, 47
	s_nop 3
	s_cmp_ge_u32 s92, 0x800
	s_cbranch_scc1 .Lpf1_done
	s_and_b32 s93, s92, 15
	s_lshl_b32 s93, s93, 7
	s_bfe_u32 s94, s92, 0x40004
	s_mul_i32 s94, s94, 0xc00000
	s_add_u32 s93, s94, s93
	s_add_u32 s64, s64, s93
	s_addc_u32 s65, s65, 0
	s_lshr_b32 s93, s92, 8
	s_sub_i32 s93, 7, s93
	s_mul_i32 s93, s93, 0x180000
	v_mbcnt_lo_u32_b32 v250, -1, 0
	v_mbcnt_hi_u32_b32 v250, -1, v250
	v_mul_u32_u24_e32 v251, 0x1800, v250
	v_add_u32_e32 v252, 0x60000, v251
	s_nop 1
	global_load_dword v253, v251, s[64:65] offset:2048
	global_load_dword v253, v252, s[64:65] offset:2048
	v_add_u32_e32 v250, 0x1000, v251
	v_add_u32_e32 v252, 0x1000, v252
	global_load_dword v253, v250, s[64:65]
	global_load_dword v253, v252, s[64:65]
	v_add_u32_e32 v251, s93, v251
	v_add_u32_e32 v252, 0x60000, v251
	global_load_dword v253, v251, s[64:65]
	global_load_dword v253, v252, s[64:65]
	v_add_u32_e32 v251, 0xc0000, v251
	v_add_u32_e32 v252, 0xc0000, v252
	global_load_dword v253, v251, s[64:65]
	global_load_dword v253, v252, s[64:65]
.Lpf1_done:
	s_cmp_eq_u32 s39, s52
	s_cselect_b64 s[0:1], -1, 0
	s_mov_b64 s[34:35], -1
	s_and_b64 vcc, exec, s[0:1]
	s_cbranch_vccnz .LBB0_3043
	v_bfe_u32 v32, v198, s39, 1
	v_cmp_ne_u32_e32 vcc, 0, v32
	s_cmp_lg_u64 vcc, 0
	s_cselect_b64 s[6:7], -1, 0
	s_lshl_b32 s34, s38, 6
	s_cbranch_execz .LBB0_3044
